# attention stream's LDS transpose tile padded to 72-byte rows (ds_write_b16 bank conflicts 8-way -> 2-way); 4608 B static LDS
# speedup vs baseline: 1.0171x; 1.0019x over previous
; #define LAS __attribute__((address_space(3)))
; #define WAIT_BAR(N) asm volatile("s_waitcnt vmcnt(" #N ") lgkmcnt(0)\n\ts_barrier" ::: "memory")
; #define DMA_K(t, slot) do { const bf16_t* sb_ = Kh + (long)(t) * KVBLK * DMK; glds16<0>(sb_, kvoff, (unsigned)__builtin_amdgcn_readfirstlane(kdst + (slot))); glds16<0>(sb_ + 64, kvoff, (unsigned)__builtin_amdgcn_readfirstlane(kdst + 8192 + (slot))); } while (0)
; template <int THRL> ...
;     ...
;   const bf16_t* Qw = Q + (size_t)(CTXL + qb * 128 + wq * QBLK) * DMK + head * 128 + comp * 64;
;   const bf16_t* Kh = K + head * 128; const bf16_t* Vh = V + head * 128;
;   const unsigned lds0 = (unsigned)(uintptr_t)shm;
;   LAS float* wsf = (LAS float*)(shm + LDS_WS) + wid * 64;
;   const unsigned kvoff = (unsigned)(lane * DMK + wid * 8) * 2u;
;   const unsigned vvoff = (unsigned)((16 * (wid & 3) + (lane >> 2)) * DMK + (wid >> 2) * 32 + (lane & 3) * 8) * 2u;
;   const unsigned kdst = lds0 + LDS_K + wid * 1024, vdst = lds0 + LDS_V + wid * 1024;
;     ...
;   const int vb0 = (int)(lds0 + LDS_V) + ((lane >> 4) & 1) * 32 + (lane & 3) * 8 + (4 * hi + ((lane & 15) >> 2)) * 64;
;   bf16x8 kf[8];
;   const lds_cptr shm3 = (lds_cptr)shm; const lds_cptr kp0 = shm3 + LDS_K + comp * 8192 + hi * 1024 + r32 * 16;
;   const lds_cptr vp0 = shm3 + LDS_V + ((lane >> 4) & 1) * 32 + (lane & 3) * 8 + (4 * hi + ((lane & 15) >> 2)) * 64;
;   DMA_K(0, 0); DMA_V(0, 0); DMA_K(1, SLOTB);
;   bf16x8 qr[4];
; #pragma unroll
;   for (int d0 = 0; d0 < 4; ++d0) qr[d0] = *reinterpret_cast<const bf16x8*>(&Qw[(long)r32 * DMK + d0 * 16 + hi * 8]);
;   float mhat = 0.f, l_reg = 0.f; f32x16 o[4]; o[0] = f32x16{}; o[1] = f32x16{}; o[2] = f32x16{}; o[3] = f32x16{}; f32x16 negm = f32x16{}; asm volatile("" : "+v"(negm));
;   bool resc = false;
;     ...
;   f32x16 pA0, pA1, pB0, pB1;
;   int sl_prev = 0, sl_cur = 0, sl_next = SLOTB;
;     ...
;   DMA_K(2, 2 * SLOTB);
;   WAIT_BAR(6);
;   qkt(pA0, pA1, kp0, qr, negm); asm volatile("s_nop 15\n\ts_nop 7" : "+v"(pA0), "+v"(pA1));
;   const lds_cptr qp = shm3 + LDS_Q + wid * 4096 + lane * 16;
; #pragma unroll
;   for (int d0 = 0; d0 < 4; ++d0) *(LAS bf16x8*)(shm + LDS_Q + wid * 4096 + lane * 16 + d0 * 1024) = qr[d0];
;   START(pA0, pA1);
; #pragma unroll
;   for (int r = 0; r < 16; ++r) pA1[r] = __builtin_amdgcn_exp2f(pA1[r]);
;   WAIT_BAR(0);
.LBB0_527:
	s_lshl_b32 s0, s28, 1
	s_and_b32 s0, s0, 0x700
	s_add_u32 s33, s26, s0
	s_addc_u32 s53, s27, 0
	s_bfe_u32 s41, s39, 0x20006
	s_lshl_b32 s0, s36, 4
	s_and_b32 s37, s0, 0xffffff80
	s_lshl_b32 s0, s41, 5
	s_or_b32 s0, s37, s0
	s_addk_i32 s0, 0x100
	s_ashr_i32 s1, s0, 31
	s_lshr_b32 s40, s39, 6
	s_lshr_b32 s42, s39, 8
	s_lshl_b64 s[0:1], s[0:1], 11
	s_add_u32 s0, s5, s0
	s_addc_u32 s1, s17, s1
	s_lshl_b32 s2, s36, 7
	s_and_b32 s14, s2, 0x380
	s_lshl_b32 s8, s14, 1
	s_add_u32 s0, s0, s8
	s_addc_u32 s1, s1, 0
	s_lshl_b32 s43, s42, 6
	s_lshl_b32 s2, s42, 7
	s_add_u32 s2, s0, s2
	s_addc_u32 s3, s1, 0
	s_add_u32 s20, s22, s8
	s_addc_u32 s21, s23, 0
	s_add_u32 s8, s24, s8
	s_addc_u32 s9, s25, 0
	s_lshl_b32 s0, s41, 15
	s_add_i32 s0, s0, s43
	v_add_u32_e32 v235, s0, v219
	s_lshl_b32 s0, s40, 10
	s_add_i32 s49, s0, 0
	s_and_b32 s1, s39, 0x3fffffc0
	s_lshl_b32 s38, s40, 4
	s_add_i32 s46, s49, 0xc000
	s_add_u32 s44, s20, 0x80
	v_add_u32_e32 v237, s38, v218
	s_mov_b32 s0, m0
	s_mov_b32 m0, s49
	s_nop 0
	global_load_lds_dwordx4 v237, s[20:21] offset:0
	s_mov_b32 m0, s0
	s_addc_u32 s45, s21, 0
	s_add_i32 s54, s49, 0x2000
	s_mov_b32 s0, m0
	s_mov_b32 m0, s54
	s_nop 0
	global_load_lds_dwordx4 v237, s[44:45] offset:0
	s_mov_b32 m0, s0
	s_add_u32 s50, s8, 0x80
	s_mov_b32 s0, m0
	s_mov_b32 m0, s46
	s_nop 0
	global_load_lds_dwordx4 v235, s[8:9] offset:0
	s_mov_b32 m0, s0
	s_addc_u32 s51, s9, 0
	s_add_i32 s45, s49, 0xe000
	s_mov_b32 s0, m0
	s_mov_b32 m0, s45
	s_nop 0
	global_load_lds_dwordx4 v235, s[50:51] offset:0
	s_mov_b32 m0, s0
	s_add_u32 s50, s20, 0x20000
	s_addc_u32 s51, s21, 0
	s_add_i32 s52, s49, 0x4000
	s_mov_b32 s0, m0
	s_mov_b32 m0, s52
	s_nop 0
	global_load_lds_dwordx4 v237, s[50:51] offset:0
	s_mov_b32 m0, s0
	s_add_u32 s56, s20, 0x20080
	s_addc_u32 s57, s21, 0
	s_add_i32 s51, s49, 0x6000
	s_mov_b32 s0, m0
	s_mov_b32 m0, s51
	s_nop 0
	global_load_lds_dwordx4 v237, s[56:57] offset:0
	s_mov_b32 m0, s0
	global_load_dwordx4 v[66:69], v229, s[2:3]
	global_load_dwordx4 v[70:73], v229, s[2:3] offset:32
	global_load_dwordx4 v[74:77], v229, s[2:3] offset:64
	global_load_dwordx4 v[78:81], v229, s[2:3] offset:96
	v_mov_b64_e32 v[48:49], v[32:33]
	s_add_u32 s2, s20, 0x40000
	v_mov_b64_e32 v[46:47], v[30:31]
	v_mov_b64_e32 v[44:45], v[28:29]
	v_mov_b64_e32 v[42:43], v[26:27]
	v_mov_b64_e32 v[40:41], v[24:25]
	v_mov_b64_e32 v[38:39], v[22:23]
	v_mov_b64_e32 v[36:37], v[20:21]
	v_mov_b64_e32 v[34:35], v[18:19]
	s_addc_u32 s3, s21, 0
	s_add_i32 s48, s49, 0x8000
	s_mov_b32 s0, m0
	s_mov_b32 m0, s48
	s_nop 0
	global_load_lds_dwordx4 v237, s[2:3] offset:0
	s_mov_b32 m0, s0
	s_add_u32 s2, s20, 0x40080
	s_addc_u32 s3, s21, 0
	s_add_i32 s47, s49, 0xa000
	s_mov_b32 s0, m0
	s_mov_b32 m0, s47
	s_nop 0
	global_load_lds_dwordx4 v237, s[2:3] offset:0
	s_mov_b32 m0, s0
	v_lshl_add_u32 v236, s42, 13, v221
	s_waitcnt vmcnt(6) lgkmcnt(0)
	s_barrier
	ds_read_b128 v[4:7], v236
	s_lshl_b32 s2, s40, 12
	v_add_u32_e32 v233, s2, v222
	s_lshl_b32 s1, s1, 2
	s_add_i32 s50, s1, 0
	s_add_i32 s50, s50, 0x18000
	s_add_u32 s2, s20, 0x60000
	s_addc_u32 s3, s21, 0
	v_mov_b32_e32 v3, v2
	v_mov_b32_e32 v12, v2
	v_mov_b32_e32 v13, v2
	s_movk_i32 s57, 0x4000
	s_mov_b32 s0, 0
	s_mov_b32 s55, 0x8000
	v_lshl_add_u32 v232, v217, 2, s50
	v_mov_b32_e32 v238, 0
	s_mov_b32 s56, -1
	s_waitcnt vmcnt(3) lgkmcnt(0)
	v_mfma_f32_32x32x16_bf16 v[50:65], v[4:7], v[66:69], v[34:49]
	ds_read_b128 v[4:7], v236 offset:512
	s_waitcnt lgkmcnt(0)
	v_mfma_f32_32x32x16_bf16 v[34:49], v[4:7], v[66:69], v[34:49]
	ds_read_b128 v[4:7], v236 offset:2048
	s_waitcnt vmcnt(2) lgkmcnt(0)
	v_mfma_f32_32x32x16_bf16 v[50:65], v[4:7], v[70:73], v[50:65]
	ds_read_b128 v[4:7], v236 offset:2560
	s_waitcnt lgkmcnt(0)
	v_mfma_f32_32x32x16_bf16 v[34:49], v[4:7], v[70:73], v[34:49]
	ds_read_b128 v[4:7], v236 offset:4096
	ds_read_b128 v[8:11], v236 offset:4608
	ds_read_b128 v[82:85], v236 offset:6656
	ds_read_b128 v[14:17], v236 offset:6144
	s_waitcnt vmcnt(1) lgkmcnt(3)
	v_mfma_f32_32x32x16_bf16 v[50:65], v[4:7], v[74:77], v[50:65]
	v_mov_b32_e32 v4, v2
	v_mov_b32_e32 v5, v2
	v_mov_b32_e32 v6, v2
	v_mov_b32_e32 v7, v2
	s_waitcnt lgkmcnt(2)
	v_mfma_f32_32x32x16_bf16 v[34:49], v[8:11], v[74:77], v[34:49]
	v_mov_b32_e32 v8, v2
	v_mov_b32_e32 v9, v2
	v_mov_b32_e32 v10, v2
	v_mov_b32_e32 v11, v2
	s_waitcnt vmcnt(0) lgkmcnt(0)
	v_mfma_f32_32x32x16_bf16 v[50:65], v[14:17], v[78:81], v[50:65]
	v_mov_b32_e32 v16, v2
	v_mov_b32_e32 v17, v2
	v_mov_b32_e32 v14, v2
	v_mov_b32_e32 v15, v2
	v_mfma_f32_32x32x16_bf16 v[34:49], v[82:85], v[78:81], v[34:49]
	s_nop 15
	s_nop 7
	ds_write_b128 v233, v[66:69]
	ds_write_b128 v233, v[70:73] offset:1024
	ds_write_b128 v233, v[74:77] offset:2048
	ds_write_b128 v233, v[78:81] offset:3072
	v_max3_f32 v66, v50, v51, v34
	v_max3_f32 v67, v52, v53, v35
	v_mov_b64_e32 v[96:97], v[16:17]
	v_max3_f32 v66, v66, v36, v37
	v_max3_f32 v67, v67, v56, v57
	v_mov_b64_e32 v[94:95], v[14:15]
	v_max3_f32 v66, v66, v54, v55
	v_max3_f32 v67, v67, v40, v41
	v_mov_b64_e32 v[92:93], v[12:13]
	v_max3_f32 v66, v66, v38, v39
	v_max3_f32 v67, v67, v60, v61
	v_mov_b64_e32 v[90:91], v[10:11]
	v_max3_f32 v66, v66, v58, v59
	v_max3_f32 v67, v67, v44, v45
	v_mov_b64_e32 v[88:89], v[8:9]
	v_max3_f32 v66, v66, v42, v43
	v_max3_f32 v67, v67, v64, v65
	v_mov_b64_e32 v[86:87], v[6:7]
	v_max3_f32 v66, v66, v62, v63
	v_max3_f32 v67, v67, v48, v49
	v_mov_b64_e32 v[84:85], v[4:5]
	v_max3_f32 v66, v66, v46, v47
	v_mov_b64_e32 v[82:83], v[2:3]
	v_max_f32_e32 v66, v66, v67
	s_nop 0
	v_mov_b32_e32 v67, v66
	s_nop 1
	v_permlane32_swap_b32_e32 v66, v67
	v_max_f32_e32 v66, v66, v67
	s_nop 0
	v_add_f32_e32 v234, v2, v66
	v_sub_f32_e32 v50, v50, v66
	v_sub_f32_e32 v34, v34, v66
	v_sub_f32_e32 v51, v51, v66
	v_sub_f32_e32 v35, v35, v66
	v_sub_f32_e32 v52, v52, v66
	s_nop 0
	v_xor_b32_e32 v98, 0x80000000, v234
	v_mov_b32_e32 v99, v98
	v_mov_b32_e32 v100, v98
	v_mov_b32_e32 v101, v98
	v_mov_b32_e32 v102, v98
	v_mov_b32_e32 v103, v98
	v_mov_b32_e32 v104, v98
	v_mov_b32_e32 v105, v98
	v_mov_b32_e32 v106, v98
	v_mov_b32_e32 v107, v98
	v_mov_b32_e32 v108, v98
	v_mov_b32_e32 v109, v98
	v_mov_b32_e32 v110, v98
	v_mov_b32_e32 v111, v98
	v_mov_b32_e32 v112, v98
	v_mov_b32_e32 v113, v98
	s_waitcnt vmcnt(0) lgkmcnt(0)
	s_barrier
; #define LAS __attribute__((address_space(3)))
; __device__ __forceinline__ unsigned pk2(float lo, float hi) { return f2bf(lo) | (f2bf(hi) << 16); }
; #define WAIT_BAR(N) asm volatile("s_waitcnt vmcnt(" #N ") lgkmcnt(0)\n\ts_barrier" ::: "memory")
; #define DMA_K(t, slot) do { const bf16_t* sb_ = Kh + (long)(t) * KVBLK * DMK; glds16<0>(sb_, kvoff, (unsigned)__builtin_amdgcn_readfirstlane(kdst + (slot))); glds16<0>(sb_ + 64, kvoff, (unsigned)__builtin_amdgcn_readfirstlane(kdst + 8192 + (slot))); } while (0)
; #define DMA_V(t, slot) do { const bf16_t* sb_ = Vh + (long)(t) * KVBLK * DMK; glds16<0>(sb_, vvoff, (unsigned)__builtin_amdgcn_readfirstlane(vdst + (slot))); glds16<0>(sb_ + 64, vvoff, (unsigned)__builtin_amdgcn_readfirstlane(vdst + 8192 + (slot))); } while (0)
; #define ROT() do { sl_prev = sl_cur; sl_cur = sl_next; sl_next = (sl_next == (NSLOT - 1) * SLOTB) ? 0 : sl_next + SLOTB; } while (0)
;     __device__ __forceinline__ const float* x() const { return (const float*)ld(0); }
;     __device__ __forceinline__ const float* c() const { return (const float*)ld(1); }
; template <int THRL> ...
;     ...
;   DMA_K(3, 0); DMA_V(1, SLOTB);
;   ROT();
;   kload8(kf, kp0 + sl_cur);
;   WAIT_BAR(4);
;   s16x4 vlo[4], vhi[4]; u32x4 pw0, pw1, pw2, pw3;
; template <bool NT = true> __device__ __forceinline__ void cvt_store(const CvtItem& d, const f32x4 (&v)[8], LAS float* scr, int lane) {
;     const int rr = lane >> 3, c4 = (lane & 7) * 4;
; #pragma unroll
;     for (int q = 0; q < 8; ++q) { LAS float* t = scr + (8 * q + rr) * 33 + c4; t[0] = v[q].x; t[1] = v[q].y; t[2] = v[q].z; t[3] = v[q].w; }
;     asm volatile("s_waitcnt lgkmcnt(0)" ::: "memory");
;     const int c = lane & 7;
; #pragma unroll
;     for (int j = 0; j < 4; ++j) { const int n = (lane >> 3) + 8 * j; const LAS float* s = scr + (8 * c) * 33 + n;
;         u32x4 o; o.x = pk2(s[0 * 33], s[1 * 33]); o.y = pk2(s[2 * 33], s[3 * 33]); o.z = pk2(s[4 * 33], s[5 * 33]); o.w = pk2(s[6 * 33], s[7 * 33]);
;         const int ng = d.n0 + n, drow = d.row_off + (d.ilv ? ((ng >> 7) * 256 + (ng & 127)) : ng);
;         if (NT) __builtin_nontemporal_store(o, (u32x4*)(d.dst + (size_t)drow * d.K + d.k0 + 8 * c)); else *(u32x4*)(d.dst + (size_t)drow * d.K + d.k0 + 8 * c) = o; }
	s_mov_b32 s1, m0
	s_mov_b32 m0, s49
	s_nop 0
	global_load_lds_dwordx4 v237, s[2:3] offset:0
	s_mov_b32 m0, s1
	s_add_u32 s2, s20, 0x60080
	s_addc_u32 s3, s21, 0
	s_mov_b32 s1, m0
	s_mov_b32 m0, s54
	s_nop 0
	global_load_lds_dwordx4 v237, s[2:3] offset:0
	s_mov_b32 m0, s1
	s_add_u32 s2, s8, 0x20000
	s_addc_u32 s3, s9, 0
	s_add_i32 s44, s49, 0x10000
	s_mov_b32 s1, m0
	s_mov_b32 m0, s44
	s_nop 0
	global_load_lds_dwordx4 v235, s[2:3] offset:0
	s_mov_b32 m0, s1
	s_add_u32 s2, s8, 0x20080
	s_addc_u32 s3, s9, 0
	s_add_i32 s43, s49, 0x12000
	s_mov_b32 s1, m0
	s_mov_b32 m0, s43
	s_nop 0
	global_load_lds_dwordx4 v235, s[2:3] offset:0
	s_mov_b32 m0, s1
	ds_read_b128 v[146:149], v236 offset:16384
	ds_read_b128 v[202:205], v236 offset:16896
	ds_read_b128 v[206:209], v236 offset:18432
	ds_read_b128 v[190:193], v236 offset:18944
	ds_read_b128 v[198:201], v236 offset:20480
	ds_read_b128 v[186:189], v236 offset:20992
	ds_read_b128 v[182:185], v236 offset:22528
	ds_read_b128 v[178:181], v236 offset:23040
	v_sub_f32_e32 v36, v36, v66
	v_sub_f32_e32 v53, v53, v66
	v_sub_f32_e32 v37, v37, v66
	v_sub_f32_e32 v54, v54, v66
	v_sub_f32_e32 v38, v38, v66
	v_sub_f32_e32 v55, v55, v66
	v_sub_f32_e32 v39, v39, v66
	v_sub_f32_e32 v56, v56, v66
	v_sub_f32_e32 v40, v40, v66
	v_sub_f32_e32 v57, v57, v66
	v_sub_f32_e32 v41, v41, v66
	v_sub_f32_e32 v58, v58, v66
	v_sub_f32_e32 v42, v42, v66
	v_sub_f32_e32 v59, v59, v66
	v_sub_f32_e32 v43, v43, v66
	v_sub_f32_e32 v60, v60, v66
	v_sub_f32_e32 v44, v44, v66
	v_sub_f32_e32 v61, v61, v66
	v_sub_f32_e32 v45, v45, v66
	v_sub_f32_e32 v62, v62, v66
	v_sub_f32_e32 v46, v46, v66
	v_sub_f32_e32 v63, v63, v66
	v_sub_f32_e32 v47, v47, v66
	v_sub_f32_e32 v64, v64, v66
	v_sub_f32_e32 v48, v48, v66
	v_sub_f32_e32 v65, v65, v66
	v_sub_f32_e32 v49, v49, v66
	v_exp_f32_e32 v130, v50
	v_exp_f32_e32 v131, v51
	v_exp_f32_e32 v132, v52
	v_exp_f32_e32 v133, v53
	v_exp_f32_e32 v134, v54
	v_exp_f32_e32 v135, v55
	v_exp_f32_e32 v136, v56
	v_exp_f32_e32 v137, v57
	v_exp_f32_e32 v138, v58
	v_exp_f32_e32 v139, v59
	v_exp_f32_e32 v140, v60
	v_exp_f32_e32 v141, v61
	v_exp_f32_e32 v142, v62
	v_exp_f32_e32 v143, v63
	v_exp_f32_e32 v144, v64
	v_exp_f32_e32 v145, v65
	v_exp_f32_e32 v114, v34
	v_exp_f32_e32 v115, v35
	v_exp_f32_e32 v116, v36
	v_exp_f32_e32 v117, v37
	v_exp_f32_e32 v118, v38
	v_exp_f32_e32 v119, v39
	v_exp_f32_e32 v120, v40
	v_exp_f32_e32 v121, v41
	v_exp_f32_e32 v122, v42
	v_exp_f32_e32 v123, v43
	v_exp_f32_e32 v124, v44
	v_exp_f32_e32 v125, v45
	v_exp_f32_e32 v126, v46
	v_exp_f32_e32 v127, v47
	v_exp_f32_e32 v128, v48
	v_exp_f32_e32 v129, v49
	s_waitcnt vmcnt(4) lgkmcnt(0)
	s_barrier
	v_mov_b64_e32 v[80:81], v[16:17]
	v_mov_b64_e32 v[48:49], v[16:17]
	v_mov_b64_e32 v[64:65], v[16:17]
	v_mov_b64_e32 v[78:79], v[14:15]
	v_mov_b64_e32 v[76:77], v[12:13]
	v_mov_b64_e32 v[74:75], v[10:11]
	v_mov_b64_e32 v[72:73], v[8:9]
	v_mov_b64_e32 v[70:71], v[6:7]
	v_mov_b64_e32 v[68:69], v[4:5]
	v_mov_b64_e32 v[66:67], v[2:3]
	v_mov_b64_e32 v[46:47], v[14:15]
	v_mov_b64_e32 v[44:45], v[12:13]
	v_mov_b64_e32 v[42:43], v[10:11]
	v_mov_b64_e32 v[40:41], v[8:9]
	v_mov_b64_e32 v[38:39], v[6:7]
	v_mov_b64_e32 v[36:37], v[4:5]
	v_mov_b64_e32 v[34:35], v[2:3]
	v_mov_b64_e32 v[62:63], v[14:15]
	v_mov_b64_e32 v[60:61], v[12:13]
	v_mov_b64_e32 v[58:59], v[10:11]
	v_mov_b64_e32 v[56:57], v[8:9]
	v_mov_b64_e32 v[54:55], v[6:7]
	v_mov_b64_e32 v[52:53], v[4:5]
	v_mov_b64_e32 v[50:51], v[2:3]
	v_mov_b32_e32 v244, 0x23ee8
	ds_read2_b64 v[250:253], v244 offset1:1
	ds_read_b64 v[254:255], v244 offset:16
	s_waitcnt lgkmcnt(0)
	v_readfirstlane_b32 s68, v250
	v_readfirstlane_b32 s69, v251
	v_readfirstlane_b32 s70, v252
	v_readfirstlane_b32 s71, v253
	v_readfirstlane_b32 s72, v254
	v_readfirstlane_b32 s73, v255
	ds_read_b64 v[250:251], v244 offset:40
	s_waitcnt lgkmcnt(0)
	v_readfirstlane_b32 s74, v250
	v_readfirstlane_b32 s75, v251
	s_add_u32 s76, s74, 0x16530000
	s_addc_u32 s77, s75, 0
	s_add_u32 s74, s74, 0xa530000
	s_addc_u32 s75, s75, 0
	v_lshrrev_b32_e32 v25, 3, v214
	v_and_b32_e32 v28, 7, v214
	v_lshlrev_b32_e32 v33, 4, v28
	v_lshl_add_u32 v24, v25, 12, v33
	v_lshl_add_u32 v246, v25, 13, v33
	v_mov_b32_e32 v29, 0x120
	v_mul_u32_u24_e32 v29, v29, v28
	v_lshl_add_u32 v29, v25, 1, v29
	s_mul_i32 s2, s40, 2304
	s_cmp_lt_u32 s40, 6
	s_mov_b32 s3, 0x20a00
	s_cselect_b32 s3, 0x20800, s3
	s_add_i32 s2, s2, s3
	v_add_u32_e32 v29, s2, v29
	v_add_u32_e32 v29, 32, v29
	v_mov_b32_e32 v32, 72
	v_mul_u32_u24_e32 v32, v32, v25
	v_lshl_add_u32 v32, v28, 3, v32
	v_add_u32_e32 v32, s2, v32
	s_mul_i32 s66, s96, 8
	s_add_i32 s66, s66, s40
	s_cmpk_lt_u32 s36, 0x100
	s_movk_i32 s67, 104
	s_cselect_b32 s67, 104, s67
	s_cselect_b32 s2, 0, 0x6800
	s_add_i32 s66, s66, s2
	s_add_i32 s90, s67, 6
	s_cmp_eq_u32 s67, 0
	s_cselect_b32 s90, -1, s90
	global_load_dword v249, v24, s[68:69]
	global_load_dword v249, v24, s[68:69]

; #define LAS __attribute__((address_space(3)))
;     __device__ __forceinline__ const float* x() const { return (const float*)ld(0); }
; template <bool NT = true> __device__ __forceinline__ void cvt_store(const CvtItem& d, const f32x4 (&v)[8], LAS float* scr, int lane) {
;     const int rr = lane >> 3, c4 = (lane & 7) * 4;
; #pragma unroll
;     for (int q = 0; q < 8; ++q) { LAS float* t = scr + (8 * q + rr) * 33 + c4; t[0] = v[q].x; t[1] = v[q].y; t[2] = v[q].z; t[3] = v[q].w; }
;     asm volatile("s_waitcnt lgkmcnt(0)" ::: "memory");
.Lcs_W_h0:
	ds_write_b16 v29, v245
	ds_write_b16_d16_hi v29, v245 offset:72
	ds_write_b16 v29, v244 offset:144
	ds_write_b16_d16_hi v29, v244 offset:216
	v_add_u32_e32 v29, 16, v29

; #define LAS __attribute__((address_space(3)))
;     __device__ __forceinline__ const float* x() const { return (const float*)ld(0); }
; template <bool NT = true> __device__ __forceinline__ void cvt_store(const CvtItem& d, const f32x4 (&v)[8], LAS float* scr, int lane) {
;     const int rr = lane >> 3, c4 = (lane & 7) * 4;
; #pragma unroll
;     for (int q = 0; q < 8; ++q) { LAS float* t = scr + (8 * q + rr) * 33 + c4; t[0] = v[q].x; t[1] = v[q].y; t[2] = v[q].z; t[3] = v[q].w; }
;     asm volatile("s_waitcnt lgkmcnt(0)" ::: "memory");
.Lcs_noL_h1:
	s_waitcnt lgkmcnt(0)
	v_mfma_f32_32x32x16_bf16 v[50:65], v[4:7], v[158:161], v[50:65]
	v_exp_f32_e32 v128, v128
	v_exp_f32_e32 v129, v129
	s_waitcnt lgkmcnt(0)
	s_cmp_gt_i32 s2, s90
	s_cbranch_scc1 .Lcs_noW_h1
	ds_write_b16 v29, v245
	ds_write_b16_d16_hi v29, v245 offset:72
	ds_write_b16 v29, v244 offset:144
	ds_write_b16_d16_hi v29, v244 offset:216
	s_bitcmp1_b32 s2, 1
	s_cselect_b32 s3, 16, -48
	v_add_u32_e32 v29, s3, v29

; #define LAS __attribute__((address_space(3)))
; __device__ __forceinline__ unsigned pk2(float lo, float hi) { return f2bf(lo) | (f2bf(hi) << 16); }
;     __device__ __forceinline__ const float* x() const { return (const float*)ld(0); }
;     __device__ __forceinline__ const float* c() const { return (const float*)ld(1); }
; template <bool NT = true> __device__ __forceinline__ void cvt_store(const CvtItem& d, const f32x4 (&v)[8], LAS float* scr, int lane) {
;     ...
;     const int c = lane & 7;
; #pragma unroll
;     for (int j = 0; j < 4; ++j) { const int n = (lane >> 3) + 8 * j; const LAS float* s = scr + (8 * c) * 33 + n;
;         u32x4 o; o.x = pk2(s[0 * 33], s[1 * 33]); o.y = pk2(s[2 * 33], s[3 * 33]); o.z = pk2(s[4 * 33], s[5 * 33]); o.w = pk2(s[6 * 33], s[7 * 33]);
;         const int ng = d.n0 + n, drow = d.row_off + (d.ilv ? ((ng >> 7) * 256 + (ng & 127)) : ng);
;         if (NT) __builtin_nontemporal_store(o, (u32x4*)(d.dst + (size_t)drow * d.K + d.k0 + 8 * c)); else *(u32x4*)(d.dst + (size_t)drow * d.K + d.k0 + 8 * c) = o; }
.Lcs_R_h0:
	ds_read_b64 v[254:255], v32
	ds_read_b64 v[30:31], v32 offset:576
	ds_read_b64 v[22:23], v32 offset:1152
	ds_read_b64 v[26:27], v32 offset:1728
	s_branch .Lcs_W_h0

; __global__ void __launch_bounds__(NTHR, 2) fwd(Args ka) {
	.amdhsa_kernel _Z3fwd4Args
		.amdhsa_group_segment_fixed_size 4608
		.amdhsa_private_segment_fixed_size 0
		.amdhsa_kernarg_size 480
		.amdhsa_user_sgpr_count 2
		.amdhsa_user_sgpr_dispatch_ptr 0
		.amdhsa_user_sgpr_queue_ptr 0
		.amdhsa_user_sgpr_kernarg_segment_ptr 1
		.amdhsa_user_sgpr_dispatch_id 0
		.amdhsa_user_sgpr_kernarg_preload_length 0
		.amdhsa_user_sgpr_kernarg_preload_offset 0
		.amdhsa_user_sgpr_private_segment_size 0
		.amdhsa_uses_dynamic_stack 0
		.amdhsa_enable_private_segment 0
		.amdhsa_system_sgpr_workgroup_id_x 1
		.amdhsa_system_sgpr_workgroup_id_y 0
		.amdhsa_system_sgpr_workgroup_id_z 0
		.amdhsa_system_sgpr_workgroup_info 0
		.amdhsa_system_vgpr_workitem_id 0
		.amdhsa_next_free_vgpr 256
		.amdhsa_next_free_sgpr 102
		.amdhsa_accum_offset 256
		.amdhsa_reserve_vcc 1
		.amdhsa_float_round_mode_32 0
		.amdhsa_float_round_mode_16_64 0
		.amdhsa_float_denorm_mode_32 3
		.amdhsa_float_denorm_mode_16_64 3
		.amdhsa_dx10_clamp 1
		.amdhsa_ieee_mode 1
		.amdhsa_fp16_overflow 0
		.amdhsa_tg_split 0
		.amdhsa_exception_fp_ieee_invalid_op 0
		.amdhsa_exception_fp_denorm_src 0
		.amdhsa_exception_fp_ieee_div_zero 0
		.amdhsa_exception_fp_ieee_overflow 0
		.amdhsa_exception_fp_ieee_underflow 0
		.amdhsa_exception_fp_ieee_inexact 0
		.amdhsa_exception_int_div_zero 0
	.end_amdhsa_kernel

; __global__ void __launch_bounds__(NTHR, 2) fwd(Args ka) {
amdhsa.kernels:
  - .agpr_count:     0
    .args:
      - .offset:         0
        .size:           224
        .value_kind:     by_value
      - .offset:         224
        .size:           4
        .value_kind:     hidden_block_count_x
      - .offset:         228
        .size:           4
        .value_kind:     hidden_block_count_y
      - .offset:         232
        .size:           4
        .value_kind:     hidden_block_count_z
      - .offset:         236
        .size:           2
        .value_kind:     hidden_group_size_x
      - .offset:         238
        .size:           2
        .value_kind:     hidden_group_size_y
      - .offset:         240
        .size:           2
        .value_kind:     hidden_group_size_z
      - .offset:         242
        .size:           2
        .value_kind:     hidden_remainder_x
      - .offset:         244
        .size:           2
        .value_kind:     hidden_remainder_y
      - .offset:         246
        .size:           2
        .value_kind:     hidden_remainder_z
      - .offset:         264
        .size:           8
        .value_kind:     hidden_global_offset_x
      - .offset:         272
        .size:           8
        .value_kind:     hidden_global_offset_y
      - .offset:         280
        .size:           8
        .value_kind:     hidden_global_offset_z
      - .offset:         288
        .size:           2
        .value_kind:     hidden_grid_dims
      - .offset:         344
        .size:           4
        .value_kind:     hidden_dynamic_lds_size
    .group_segment_fixed_size: 4608
    .kernarg_segment_align: 8
    .kernarg_segment_size: 480
    .language:       OpenCL C
    .language_version:
      - 2
      - 0
    .max_flat_workgroup_size: 512
    .name:           _Z3fwd4Args
    .private_segment_fixed_size: 0
    .sgpr_count:     108
    .sgpr_spill_count: 25
    .symbol:         _Z3fwd4Args.kd
    .uniform_work_group_size: 1
    .uses_dynamic_stack: false
    .vgpr_count:     256
    .vgpr_spill_count: 0
    .wavefront_size: 64
